# prologue: 2 static conversion rounds and 4608 items through the work counter (was 3 static + 2560), Fourier-weight fold per SIMD in rounds 0/1
# speedup vs baseline: 1.0083x; 1.0042x over previous
.LBB0_41:
	v_writelane_b32 v253, s24, 32
	v_writelane_b32 v253, s23, 34
	v_writelane_b32 v253, s22, 36
	s_mov_b32 s3, 0
	v_readlane_b32 s0, v253, 29
	s_lshl_b32 s0, s0, 14
	s_add_i32 s29, s0, 0
	s_cmp_lg_u64 s[48:49], 0
	v_readlane_b32 s4, v253, 30
	s_cselect_b64 s[44:45], -1, 0
	s_abs_i32 s2, s4
	v_cvt_f32_u32_e32 v2, s2
	s_sub_i32 s0, 0, s2
	s_ashr_i32 s6, s4, 31
	v_rcp_iflag_f32_e32 v2, v2
	s_nop 0
	v_mul_f32_e32 v2, 0x4f7ffffe, v2
	v_cvt_u32_f32_e32 v2, v2
	s_nop 0
	v_readfirstlane_b32 s1, v2
	s_mul_i32 s0, s0, s1
	s_mul_hi_u32 s0, s1, s0
	s_add_i32 s7, s1, s0
	s_mul_hi_u32 s0, s7, 0x4200
	s_mul_i32 s0, s0, s2
	s_sub_i32 s0, 0x4200, s0
	s_sub_i32 s1, s0, s2
	s_cmp_ge_u32 s0, s2
	s_cselect_b32 s0, s1, s0
	s_sub_i32 s1, s0, s2
	s_cmp_ge_u32 s0, s2
	s_cselect_b32 s8, s1, s0
	s_add_i32 s0, s4, 0xffffff00
	s_cmp_ge_i32 s0, s8
	s_cselect_b64 s[0:1], -1, 0
	s_cmpk_lt_u32 s8, 0x2101
	s_cselect_b64 s[4:5], -1, 0
	s_sub_i32 s8, 0x4200, s8
	s_and_b64 s[0:1], s[0:1], s[4:5]
	s_and_b64 s[0:1], s[0:1], exec
	s_cselect_b32 s5, s8, 0x4200
	s_add_i32 s0, s5, 0xffffe200
	s_cmp_eq_u32 s2, 0x800
	s_cselect_b32 s5, s0, s5
	v_writelane_b32 v253, s5, 38
	v_writelane_b32 v253, s48, 40
	s_mul_hi_u32 s0, s5, s7
	s_mul_i32 s1, s0, s2
	v_writelane_b32 v253, s49, 41
	v_writelane_b32 v253, s50, 42
	v_writelane_b32 v253, s51, 43
	v_writelane_b32 v253, s52, 44
	v_writelane_b32 v253, s53, 45
	v_writelane_b32 v253, s54, 46
	v_writelane_b32 v253, s55, 47
	s_sub_i32 s1, s5, s1
	v_writelane_b32 v253, s56, 48
	s_add_i32 s4, s0, 1
	s_sub_i32 s5, s1, s2
	v_writelane_b32 v253, s57, 49
	s_cmp_ge_u32 s1, s2
	v_writelane_b32 v253, s58, 50
	s_cselect_b32 s0, s4, s0
	v_writelane_b32 v253, s59, 51
	s_cselect_b32 s1, s5, s1
	s_add_i32 s4, s0, 1
	v_writelane_b32 v253, s60, 52
	s_cmp_ge_u32 s1, s2
	v_writelane_b32 v253, s61, 53
	s_cselect_b32 s0, s4, s0
	v_writelane_b32 v253, s62, 54
	s_xor_b32 s0, s0, s6
	v_writelane_b32 v253, s63, 55
	s_sub_i32 s15, s0, s6
	v_writelane_b32 v253, s29, 56
	s_add_i32 s14, s15, -2
	v_writelane_b32 v253, s44, 57
	s_cmp_lt_i32 s15, 1
	v_readfirstlane_b32 s0, v0
	v_writelane_b32 v253, s45, 58
	s_cbranch_scc1 .LBB0_65
	s_ashr_i32 s0, s0, 8
	s_min_i32 s18, s0, s14
	s_cmpk_gt_i32 s27, 0x7ff
	v_readlane_b32 s0, v253, 26
	s_cselect_b64 s[20:21], -1, 0
	s_add_u32 s0, s0, 0x800000
	v_writelane_b32 v253, s0, 59
	v_mov_b32_e32 v133, 0
	v_readlane_b32 s0, v253, 27
	s_addc_u32 s0, s0, 0
	s_add_i32 s25, 0, 0x21000
	v_writelane_b32 v253, s0, 61
	s_add_i32 s0, 0, 0x21200
	v_writelane_b32 v253, s0, 63
	s_add_i32 s0, 0, 0x21100
	v_writelane_b32 v254, s0, 1
	s_add_i32 s0, 0, 0x21300
	v_writelane_b32 v254, s0, 3
	v_writelane_b32 v254, s27, 5
	v_writelane_b32 v254, s14, 7
	v_writelane_b32 v254, s15, 9
	v_writelane_b32 v254, s18, 11
	v_writelane_b32 v254, s20, 13
	s_mov_b32 s22, 0x42800000
	s_mov_b32 s19, 0
	v_writelane_b32 v254, s21, 14
	s_branch .LBB0_45
